# speedup vs baseline: 1.0038x; 1.0038x over previous
.LBB2_9:
	v_mad_i64_i32 v[0:1], s[12:13], v110, 48, 0
	v_or_b32_e32 v0, v0, v108
	v_lshlrev_b64 v[0:1], 8, v[0:1]
	v_lshl_add_u64 v[0:1], v[114:115], 0, v[0:1]
	v_add_co_u32_e32 v2, vcc, s15, v0
	global_load_dwordx4 v[24:27], v[0:1], off nt
	global_load_dwordx4 v[20:23], v[0:1], off offset:64 nt
	global_load_dwordx4 v[16:19], v[0:1], off offset:128 nt
	global_load_dwordx4 v[12:15], v[0:1], off offset:192 nt
	v_addc_co_u32_e32 v3, vcc, 0, v1, vcc
	v_add_co_u32_e32 v0, vcc, 0x2000, v0
	v_ashrrev_i32_e32 v111, 31, v110
	s_nop 0
	v_addc_co_u32_e32 v1, vcc, 0, v1, vcc
	global_load_dwordx4 v[64:67], v[2:3], off nt
	global_load_dwordx4 v[56:59], v[2:3], off offset:64 nt
	global_load_dwordx4 v[40:43], v[2:3], off offset:128 nt
	global_load_dwordx4 v[28:31], v[2:3], off offset:192 nt
	global_load_dwordx4 v[68:71], v[0:1], off nt
	global_load_dwordx4 v[60:63], v[0:1], off offset:64 nt
	global_load_dwordx4 v[44:47], v[0:1], off offset:128 nt
	global_load_dwordx4 v[32:35], v[0:1], off offset:192 nt
	s_mov_b32 s12, 11
	v_mov_b32_e32 v72, v116
	s_mov_b32 s13, 0
	v_mov_b32_e32 v73, v109
	v_add_u32_e32 v121, v109, v112
	v_add_u32_e32 v122, 0x1f200, v112
	v_add_u32_e32 v124, v116, v112
	v_add_u32_e32 v124, 0x17600, v124
	v_mov_b32_e32 v0, 0
	v_mov_b32_e32 v1, v113
	v_mov_b32_e32 v2, v113
	v_mov_b32_e32 v3, v113
	v_mov_b32_e32 v36, 0
	v_mov_b32_e32 v37, v113
	v_mov_b32_e32 v38, v113
	v_mov_b32_e32 v39, v113
	v_mov_b32_e32 v48, 0
	v_mov_b32_e32 v49, v113
	v_mov_b32_e32 v50, v113
	v_mov_b32_e32 v51, v113
	v_mov_b32_e32 v52, 0
	v_mov_b32_e32 v53, v113
	v_mov_b32_e32 v54, v113
	v_mov_b32_e32 v55, v113
	v_mov_b32_e32 v4, 0
	v_mov_b32_e32 v5, v113
	v_mov_b32_e32 v6, v113
	v_mov_b32_e32 v7, v113
	v_mov_b32_e32 v8, 0
	v_mov_b32_e32 v9, v113
	v_mov_b32_e32 v10, v113
	v_mov_b32_e32 v11, v113
.LBB2_10:
	s_setprio 0
	ds_read_b128 v[74:77], v121
	ds_read_b128 v[78:81], v122
	ds_read_b128 v[82:85], v121 offset:64
	s_waitcnt vmcnt(11) lgkmcnt(0)
	v_mfma_f32_16x16x32_bf16 v[86:89], v[74:77], v[24:27], v[78:81]
	s_waitcnt vmcnt(7)
	v_mfma_f32_16x16x32_bf16 v[90:93], v[74:77], v[64:67], v[78:81]
	s_waitcnt vmcnt(3)
	v_mfma_f32_16x16x32_bf16 v[74:77], v[74:77], v[68:71], v[78:81]
	v_mfma_f32_16x16x32_bf16 v[78:81], v[82:85], v[20:23], v[86:89]
	v_mfma_f32_16x16x32_bf16 v[86:89], v[82:85], v[56:59], v[90:93]
	s_waitcnt vmcnt(2)
	v_mfma_f32_16x16x32_bf16 v[74:77], v[82:85], v[60:63], v[74:77]
	ds_read_b128 v[82:85], v121 offset:128
	s_nop 0
	ds_read_b128 v[90:93], v121 offset:192
	s_waitcnt lgkmcnt(1)
	v_mfma_f32_16x16x32_bf16 v[86:89], v[82:85], v[40:43], v[86:89]
	v_mfma_f32_16x16x32_bf16 v[78:81], v[82:85], v[16:19], v[78:81]
	s_waitcnt vmcnt(1)
	v_mfma_f32_16x16x32_bf16 v[74:77], v[82:85], v[44:47], v[74:77]
	s_waitcnt lgkmcnt(0)
	v_mfma_f32_16x16x32_bf16 v[82:85], v[90:93], v[28:31], v[86:89]
	s_nop 2
	ds_read_b128 v[86:89], v121 offset:4352
	v_mfma_f32_16x16x32_bf16 v[78:81], v[90:93], v[12:15], v[78:81]
	s_waitcnt vmcnt(0)
	v_mfma_f32_16x16x32_bf16 v[74:77], v[90:93], v[32:35], v[74:77]
	ds_read_b128 v[90:93], v122 offset:64
	ds_read_b128 v[94:97], v121 offset:4416
	s_waitcnt lgkmcnt(1)
	v_mfma_f32_16x16x32_bf16 v[98:101], v[86:89], v[24:27], v[90:93]
	v_mfma_f32_16x16x32_bf16 v[102:105], v[86:89], v[64:67], v[90:93]
	v_mfma_f32_16x16x32_bf16 v[86:89], v[86:89], v[68:71], v[90:93]
	s_waitcnt lgkmcnt(0)
	v_mfma_f32_16x16x32_bf16 v[90:93], v[94:97], v[20:23], v[98:101]
	v_mfma_f32_16x16x32_bf16 v[98:101], v[94:97], v[56:59], v[102:105]
	v_mfma_f32_16x16x32_bf16 v[86:89], v[94:97], v[60:63], v[86:89]
	ds_read_b128 v[94:97], v121 offset:4480
	s_nop 1
	ds_read_b128 v[102:105], v121 offset:4544
	s_waitcnt lgkmcnt(1)
	v_mfma_f32_16x16x32_bf16 v[90:93], v[94:97], v[16:19], v[90:93]
	v_mfma_f32_16x16x32_bf16 v[98:101], v[94:97], v[40:43], v[98:101]
	v_mfma_f32_16x16x32_bf16 v[86:89], v[94:97], v[44:47], v[86:89]
	s_waitcnt lgkmcnt(0)
	v_mfma_f32_16x16x32_bf16 v[90:93], v[102:105], v[12:15], v[90:93]
	v_mfma_f32_16x16x32_bf16 v[94:97], v[102:105], v[28:31], v[98:101]
	v_mfma_f32_16x16x32_bf16 v[86:89], v[102:105], v[32:35], v[86:89]
	s_setprio 2
	s_nop 1
	v_exp_f32_e32 v99, v78
	v_exp_f32_e32 v100, v79
	v_exp_f32_e32 v101, v80
	v_exp_f32_e32 v102, v81
	v_exp_f32_e32 v90, v90
	v_exp_f32_e32 v91, v91
	v_exp_f32_e32 v92, v92
	v_exp_f32_e32 v93, v93
	v_exp_f32_e32 v103, v74
	v_exp_f32_e32 v104, v75
	v_exp_f32_e32 v105, v76
	v_exp_f32_e32 v106, v77
	v_exp_f32_e32 v88, v88
	v_exp_f32_e32 v89, v89
	v_exp_f32_e32 v82, v82
	v_exp_f32_e32 v83, v83
	v_exp_f32_e32 v84, v84
	v_exp_f32_e32 v85, v85
	v_add_f32_e32 v98, 1.0, v99
	v_add_f32_e32 v99, 1.0, v100
	v_add_f32_e32 v100, 1.0, v101
	v_add_f32_e32 v101, 1.0, v102
	v_add_f32_e32 v90, 1.0, v90
	v_add_f32_e32 v91, 1.0, v91
	v_add_f32_e32 v92, 1.0, v92
	v_add_f32_e32 v93, 1.0, v93
	v_exp_f32_e32 v94, v94
	v_exp_f32_e32 v95, v95
	v_exp_f32_e32 v96, v96
	v_exp_f32_e32 v97, v97
	v_exp_f32_e32 v86, v86
	v_exp_f32_e32 v87, v87
	ds_read_b128 v[74:77], v124
	ds_read_b128 v[78:81], v124 offset:11520
	v_add_f32_e32 v102, 1.0, v103
	v_add_f32_e32 v103, 1.0, v104
	v_add_f32_e32 v104, 1.0, v105
	v_add_f32_e32 v105, 1.0, v106
	v_add_f32_e32 v106, 1.0, v88
	v_add_f32_e32 v107, 1.0, v89
	v_rcp_f32_e32 v88, v98
	v_rcp_f32_e32 v89, v99
	v_rcp_f32_e32 v98, v100
	v_rcp_f32_e32 v99, v101
	v_rcp_f32_e32 v90, v90
	v_rcp_f32_e32 v91, v91
	v_rcp_f32_e32 v92, v92
	v_rcp_f32_e32 v93, v93
	v_add_f32_e32 v82, 1.0, v82
	v_add_f32_e32 v83, 1.0, v83
	v_add_f32_e32 v84, 1.0, v84
	v_add_f32_e32 v85, 1.0, v85
	v_add_f32_e32 v94, 1.0, v94
	v_add_f32_e32 v95, 1.0, v95
	v_add_f32_e32 v96, 1.0, v96
	v_add_f32_e32 v97, 1.0, v97
	v_add_f32_e32 v86, 1.0, v86
	v_add_f32_e32 v87, 1.0, v87
	v_rcp_f32_e32 v100, v82
	v_rcp_f32_e32 v101, v83
	v_rcp_f32_e32 v119, v84
	v_rcp_f32_e32 v120, v85
	v_cvt_pk_bf16_f32 v82, v88, v89
	v_cvt_pk_bf16_f32 v83, v98, v99
	v_cvt_pk_bf16_f32 v84, v90, v91
	v_cvt_pk_bf16_f32 v85, v92, v93
	v_rcp_f32_e32 v94, v94
	v_rcp_f32_e32 v95, v95
	v_rcp_f32_e32 v96, v96
	v_rcp_f32_e32 v97, v97
	v_rcp_f32_e32 v102, v102
	v_rcp_f32_e32 v103, v103
	v_rcp_f32_e32 v104, v104
	v_rcp_f32_e32 v105, v105
	s_waitcnt lgkmcnt(1)
	v_mfma_f32_16x16x32_bf16 v[52:55], v[74:77], v[82:85], v[52:55]
	v_rcp_f32_e32 v90, v86
	v_rcp_f32_e32 v91, v87
	v_rcp_f32_e32 v92, v107
	s_waitcnt lgkmcnt(0)
	v_mfma_f32_16x16x32_bf16 v[0:3], v[78:81], v[82:85], v[0:3]
	v_rcp_f32_e32 v85, v106
	v_cvt_pk_bf16_f32 v86, v100, v101
	v_cvt_pk_bf16_f32 v87, v119, v120
	v_cvt_pk_bf16_f32 v88, v94, v95
	v_cvt_pk_bf16_f32 v89, v96, v97
	v_cvt_pk_bf16_f32 v82, v102, v103
	v_cvt_pk_bf16_f32 v83, v104, v105
	v_cvt_pk_bf16_f32 v84, v90, v91
	v_cvt_pk_bf16_f32 v85, v85, v92
	v_mfma_f32_16x16x32_bf16 v[48:51], v[74:77], v[86:89], v[48:51]
	s_add_i32 s12, s12, -1
	v_add_u32_e32 v121, 0x2200, v121
	v_add_u32_e32 v122, 0x80, v122
	v_mfma_f32_16x16x32_bf16 v[4:7], v[78:81], v[86:89], v[4:7]
	s_cmp_eq_u32 s12, 0
	v_add_u32_e32 v124, 64, v124
	v_mfma_f32_16x16x32_bf16 v[36:39], v[74:77], v[82:85], v[36:39]
	v_mfma_f32_16x16x32_bf16 v[8:11], v[78:81], v[82:85], v[8:11]
	s_cbranch_scc0 .LBB2_10
	ds_read_b128 v[72:75], v117
	ds_read_b128 v[76:79], v117 offset:64
	s_waitcnt lgkmcnt(1)
	v_mfma_f32_16x16x32_bf16 v[80:83], v[72:75], v[24:27], 0
	v_mfma_f32_16x16x32_bf16 v[84:87], v[72:75], v[64:67], 0
	v_mfma_f32_16x16x32_bf16 v[72:75], v[72:75], v[68:71], 0
	s_waitcnt lgkmcnt(0)
	v_mfma_f32_16x16x32_bf16 v[88:91], v[76:79], v[20:23], v[80:83]
	s_nop 3
	ds_read_b128 v[80:83], v117 offset:128
	ds_read_b128 v[96:99], v117 offset:192
	v_mfma_f32_16x16x32_bf16 v[84:87], v[76:79], v[56:59], v[84:87]
	v_mfma_f32_16x16x32_bf16 v[100:103], v[76:79], v[60:63], v[72:75]
	s_nop 2
	v_add_u32_e32 v72, 0, v112
	v_add_u32_e32 v92, 0x1f780, v72
	ds_read_b128 v[72:75], v92
	s_waitcnt lgkmcnt(2)
	v_mfma_f32_16x16x32_bf16 v[84:87], v[80:83], v[40:43], v[84:87]
	s_waitcnt lgkmcnt(0)
	v_add_f32_e32 v52, v72, v52
	v_mfma_f32_16x16x32_bf16 v[104:107], v[80:83], v[16:19], v[88:91]
	v_add_f32_e32 v48, v72, v48
	v_exp_f32_e32 v52, v52
	v_exp_f32_e32 v48, v48
	v_mfma_f32_16x16x32_bf16 v[80:83], v[80:83], v[44:47], v[100:103]
	v_add_f32_e32 v36, v72, v36
	v_exp_f32_e32 v36, v36
	v_add_f32_e32 v72, v52, v48
	v_mfma_f32_16x16x32_bf16 v[84:87], v[96:99], v[28:31], v[84:87]
	ds_read_b128 v[88:91], v117 offset:4352
	ds_read_b128 v[76:79], v117 offset:4416
	ds_read_b128 v[92:95], v92 offset:64
	v_add_f32_e32 v72, v72, v36
	v_add_f32_e32 v49, v73, v49
	v_mfma_f32_16x16x32_bf16 v[100:103], v[96:99], v[12:15], v[104:107]
	s_nop 1
	v_mul_f32_e32 v48, v48, v84
	v_exp_f32_e32 v49, v49
	v_add_f32_e32 v37, v73, v37
	v_mfma_f32_16x16x32_bf16 v[80:83], v[96:99], v[32:35], v[80:83]
	v_exp_f32_e32 v37, v37
	s_nop 0
	v_fmac_f32_e32 v48, v52, v100
	v_add_f32_e32 v52, v73, v53
	v_exp_f32_e32 v52, v52
	s_waitcnt lgkmcnt(2)
	v_mfma_f32_16x16x32_bf16 v[24:27], v[88:91], v[24:27], 0
	s_nop 0
	v_fmac_f32_e32 v48, v36, v80
	v_add_f32_dpp v36, v72, v72 quad_perm:[1,0,3,2] row_mask:0xf bank_mask:0xf bound_ctrl:1
	ds_read_b128 v[104:107], v117 offset:4480
	ds_read_b128 v[120:123], v117 offset:4544
	v_add_f32_dpp v36, v36, v36 quad_perm:[2,3,0,1] row_mask:0xf bank_mask:0xf bound_ctrl:1
	v_add_f32_dpp v48, v48, v48 quad_perm:[1,0,3,2] row_mask:0xf bank_mask:0xf bound_ctrl:1
	v_mfma_f32_16x16x32_bf16 v[64:67], v[88:91], v[64:67], 0
	v_add_f32_dpp v36, v36, v36 row_half_mirror row_mask:0xf bank_mask:0xf bound_ctrl:1
	v_add_f32_dpp v48, v48, v48 quad_perm:[2,3,0,1] row_mask:0xf bank_mask:0xf bound_ctrl:1
	v_add_f32_e32 v50, v74, v50
	v_add_f32_dpp v36, v36, v36 row_mirror row_mask:0xf bank_mask:0xf bound_ctrl:1
	v_rcp_f32_e32 v36, v36
	v_add_f32_dpp v48, v48, v48 row_half_mirror row_mask:0xf bank_mask:0xf bound_ctrl:1
	s_waitcnt lgkmcnt(3)
	v_mfma_f32_16x16x32_bf16 v[20:23], v[76:79], v[20:23], v[24:27]
	v_exp_f32_e32 v50, v50
	v_add_f32_dpp v48, v48, v48 row_mirror row_mask:0xf bank_mask:0xf bound_ctrl:1
	v_fma_f32 v36, v36, v48, 0
	v_add_f32_e32 v48, v52, v49
	v_mul_f32_e32 v49, v49, v85
	v_add_f32_e32 v48, v48, v37
	v_fmac_f32_e32 v49, v52, v101
	v_fmac_f32_e32 v49, v37, v81
	v_mfma_f32_16x16x32_bf16 v[68:71], v[88:91], v[68:71], 0
	v_add_f32_dpp v37, v48, v48 quad_perm:[1,0,3,2] row_mask:0xf bank_mask:0xf bound_ctrl:1
	v_add_f32_dpp v24, v49, v49 quad_perm:[1,0,3,2] row_mask:0xf bank_mask:0xf bound_ctrl:1
	v_add_f32_e32 v49, v74, v54
	v_add_f32_dpp v37, v37, v37 quad_perm:[2,3,0,1] row_mask:0xf bank_mask:0xf bound_ctrl:1
	v_add_f32_dpp v48, v24, v24 quad_perm:[2,3,0,1] row_mask:0xf bank_mask:0xf bound_ctrl:1
	v_mfma_f32_16x16x32_bf16 v[24:27], v[76:79], v[56:59], v[64:67]
	v_add_f32_dpp v37, v37, v37 row_half_mirror row_mask:0xf bank_mask:0xf bound_ctrl:1
	v_exp_f32_e32 v49, v49
	v_add_f32_dpp v48, v48, v48 row_half_mirror row_mask:0xf bank_mask:0xf bound_ctrl:1
	v_add_f32_dpp v37, v37, v37 row_mirror row_mask:0xf bank_mask:0xf bound_ctrl:1
	s_waitcnt lgkmcnt(1)
	v_mfma_f32_16x16x32_bf16 v[16:19], v[104:107], v[16:19], v[20:23]
	v_rcp_f32_e32 v37, v37
	v_add_f32_dpp v48, v48, v48 row_mirror row_mask:0xf bank_mask:0xf bound_ctrl:1
	v_add_f32_e32 v0, v92, v0
	v_add_f32_e32 v20, v74, v38
	v_mfma_f32_16x16x32_bf16 v[56:59], v[76:79], v[60:63], v[68:71]
	v_exp_f32_e32 v38, v20
	v_fmac_f32_e32 v36, v37, v48
	v_add_f32_e32 v4, v92, v4
	v_mfma_f32_16x16x32_bf16 v[20:23], v[104:107], v[40:43], v[24:27]
	v_mul_f32_e32 v40, v50, v86
	v_fmac_f32_e32 v40, v49, v102
	v_fmac_f32_e32 v40, v38, v82
	v_add_f32_e32 v24, v49, v50
	v_add_f32_e32 v37, v24, v38
	v_mfma_f32_16x16x32_bf16 v[24:27], v[104:107], v[44:47], v[56:59]
	v_exp_f32_e32 v0, v0
	v_exp_f32_e32 v4, v4
	v_add_f32_e32 v8, v92, v8
	s_waitcnt lgkmcnt(0)
	v_mfma_f32_16x16x32_bf16 v[12:15], v[120:123], v[12:15], v[16:19]
	v_exp_f32_e32 v8, v8
	v_add_f32_e32 v1, v93, v1
	v_add_f32_e32 v5, v93, v5
	v_add_f32_dpp v16, v37, v37 quad_perm:[1,0,3,2] row_mask:0xf bank_mask:0xf bound_ctrl:1
	v_exp_f32_e32 v1, v1
	v_exp_f32_e32 v5, v5
	v_add_f32_dpp v16, v16, v16 quad_perm:[2,3,0,1] row_mask:0xf bank_mask:0xf bound_ctrl:1
	v_add_f32_e32 v2, v94, v2
	v_exp_f32_e32 v2, v2
	v_add_f32_dpp v37, v16, v16 row_half_mirror row_mask:0xf bank_mask:0xf bound_ctrl:1
	v_mfma_f32_16x16x32_bf16 v[16:19], v[120:123], v[28:31], v[20:23]
	s_nop 0
	v_add_f32_dpp v28, v37, v37 row_mirror row_mask:0xf bank_mask:0xf bound_ctrl:1
	s_nop 0
	v_add_f32_dpp v20, v40, v40 quad_perm:[1,0,3,2] row_mask:0xf bank_mask:0xf bound_ctrl:1
	s_nop 1
	v_add_f32_dpp v29, v20, v20 quad_perm:[2,3,0,1] row_mask:0xf bank_mask:0xf bound_ctrl:1
	v_mfma_f32_16x16x32_bf16 v[20:23], v[120:123], v[32:35], v[24:27]
	s_nop 2
	v_add_f32_e32 v26, v75, v55
	v_add_f32_e32 v27, v75, v51
	v_rcp_f32_e32 v25, v28
	v_exp_f32_e32 v26, v26
	v_exp_f32_e32 v27, v27
	v_add_f32_e32 v28, v75, v39
	v_exp_f32_e32 v28, v28
	v_add_f32_dpp v24, v29, v29 row_half_mirror row_mask:0xf bank_mask:0xf bound_ctrl:1
	s_nop 1
	v_add_f32_dpp v24, v24, v24 row_mirror row_mask:0xf bank_mask:0xf bound_ctrl:1
	v_fmac_f32_e32 v36, v25, v24
	v_add_f32_e32 v24, v26, v27
	v_add_f32_e32 v24, v24, v28
	v_mul_f32_e32 v25, v27, v87
	v_fmac_f32_e32 v25, v26, v103
	v_add_f32_dpp v24, v24, v24 quad_perm:[1,0,3,2] row_mask:0xf bank_mask:0xf bound_ctrl:1
	v_fmac_f32_e32 v25, v28, v83
	s_nop 0
	v_add_f32_dpp v24, v24, v24 quad_perm:[2,3,0,1] row_mask:0xf bank_mask:0xf bound_ctrl:1
	v_add_f32_dpp v25, v25, v25 quad_perm:[1,0,3,2] row_mask:0xf bank_mask:0xf bound_ctrl:1
	s_nop 0
	v_add_f32_dpp v24, v24, v24 row_half_mirror row_mask:0xf bank_mask:0xf bound_ctrl:1
	v_add_f32_dpp v25, v25, v25 quad_perm:[2,3,0,1] row_mask:0xf bank_mask:0xf bound_ctrl:1
	s_nop 0
	v_add_f32_dpp v24, v24, v24 row_mirror row_mask:0xf bank_mask:0xf bound_ctrl:1
	v_rcp_f32_e32 v24, v24
	v_add_f32_dpp v25, v25, v25 row_half_mirror row_mask:0xf bank_mask:0xf bound_ctrl:1
	s_nop 1
	v_add_f32_dpp v25, v25, v25 row_mirror row_mask:0xf bank_mask:0xf bound_ctrl:1
	v_fmac_f32_e32 v36, v24, v25
	v_add_f32_e32 v24, v0, v4
	v_add_f32_e32 v24, v24, v8
	v_mul_f32_e32 v4, v4, v16
	v_fmac_f32_e32 v4, v0, v12
	v_add_f32_dpp v0, v24, v24 quad_perm:[1,0,3,2] row_mask:0xf bank_mask:0xf bound_ctrl:1
	v_fmac_f32_e32 v4, v8, v20
	v_add_f32_e32 v8, v93, v9
	v_add_f32_dpp v0, v0, v0 quad_perm:[2,3,0,1] row_mask:0xf bank_mask:0xf bound_ctrl:1
	v_add_f32_dpp v4, v4, v4 quad_perm:[1,0,3,2] row_mask:0xf bank_mask:0xf bound_ctrl:1
	v_exp_f32_e32 v8, v8
	v_add_f32_dpp v0, v0, v0 row_half_mirror row_mask:0xf bank_mask:0xf bound_ctrl:1
	v_add_f32_dpp v4, v4, v4 quad_perm:[2,3,0,1] row_mask:0xf bank_mask:0xf bound_ctrl:1
	s_nop 0
	v_add_f32_dpp v0, v0, v0 row_mirror row_mask:0xf bank_mask:0xf bound_ctrl:1
	v_rcp_f32_e32 v0, v0
	v_add_f32_dpp v4, v4, v4 row_half_mirror row_mask:0xf bank_mask:0xf bound_ctrl:1
	s_nop 1
	v_add_f32_dpp v4, v4, v4 row_mirror row_mask:0xf bank_mask:0xf bound_ctrl:1
	v_fmac_f32_e32 v36, v0, v4
	v_add_f32_e32 v0, v1, v5
	v_add_f32_e32 v0, v0, v8
	v_mul_f32_e32 v4, v5, v17
	v_fmac_f32_e32 v4, v1, v13
	v_add_f32_dpp v0, v0, v0 quad_perm:[1,0,3,2] row_mask:0xf bank_mask:0xf bound_ctrl:1
	v_fmac_f32_e32 v4, v8, v21
	v_add_f32_e32 v5, v94, v10
	v_add_f32_dpp v0, v0, v0 quad_perm:[2,3,0,1] row_mask:0xf bank_mask:0xf bound_ctrl:1
	v_add_f32_dpp v1, v4, v4 quad_perm:[1,0,3,2] row_mask:0xf bank_mask:0xf bound_ctrl:1
	v_add_f32_e32 v4, v94, v6
	v_add_f32_dpp v0, v0, v0 row_half_mirror row_mask:0xf bank_mask:0xf bound_ctrl:1
	v_exp_f32_e32 v4, v4
	v_add_f32_dpp v1, v1, v1 quad_perm:[2,3,0,1] row_mask:0xf bank_mask:0xf bound_ctrl:1
	v_add_f32_dpp v0, v0, v0 row_mirror row_mask:0xf bank_mask:0xf bound_ctrl:1
	v_rcp_f32_e32 v0, v0
	v_exp_f32_e32 v5, v5
	v_add_f32_dpp v1, v1, v1 row_half_mirror row_mask:0xf bank_mask:0xf bound_ctrl:1
	s_nop 1
	v_add_f32_dpp v1, v1, v1 row_mirror row_mask:0xf bank_mask:0xf bound_ctrl:1
	v_fmac_f32_e32 v36, v0, v1
	v_add_f32_e32 v0, v2, v4
	v_add_f32_e32 v0, v0, v5
	v_mul_f32_e32 v1, v4, v18
	v_fmac_f32_e32 v1, v2, v14
	v_add_f32_dpp v0, v0, v0 quad_perm:[1,0,3,2] row_mask:0xf bank_mask:0xf bound_ctrl:1
	v_fmac_f32_e32 v1, v5, v22
	v_add_f32_e32 v2, v95, v3
	v_add_f32_dpp v0, v0, v0 quad_perm:[2,3,0,1] row_mask:0xf bank_mask:0xf bound_ctrl:1
	v_add_f32_e32 v3, v95, v7
	v_add_f32_dpp v1, v1, v1 quad_perm:[1,0,3,2] row_mask:0xf bank_mask:0xf bound_ctrl:1
	v_add_f32_dpp v0, v0, v0 row_half_mirror row_mask:0xf bank_mask:0xf bound_ctrl:1
	v_exp_f32_e32 v2, v2
	v_exp_f32_e32 v3, v3
	v_add_f32_dpp v0, v0, v0 row_mirror row_mask:0xf bank_mask:0xf bound_ctrl:1
	v_rcp_f32_e32 v0, v0
	v_add_f32_e32 v4, v95, v11
	v_add_f32_dpp v1, v1, v1 quad_perm:[2,3,0,1] row_mask:0xf bank_mask:0xf bound_ctrl:1
	v_exp_f32_e32 v4, v4
	s_nop 0
	v_add_f32_dpp v1, v1, v1 row_half_mirror row_mask:0xf bank_mask:0xf bound_ctrl:1
	s_nop 1
	v_add_f32_dpp v1, v1, v1 row_mirror row_mask:0xf bank_mask:0xf bound_ctrl:1
	v_fmac_f32_e32 v36, v0, v1
	v_add_f32_e32 v0, v2, v3
	v_add_f32_e32 v0, v0, v4
	v_mul_f32_e32 v1, v3, v19
	v_fmac_f32_e32 v1, v2, v15
	v_add_f32_dpp v0, v0, v0 quad_perm:[1,0,3,2] row_mask:0xf bank_mask:0xf bound_ctrl:1
	v_fmac_f32_e32 v1, v4, v23
	s_nop 0
	v_add_f32_dpp v0, v0, v0 quad_perm:[2,3,0,1] row_mask:0xf bank_mask:0xf bound_ctrl:1
	v_add_f32_dpp v1, v1, v1 quad_perm:[1,0,3,2] row_mask:0xf bank_mask:0xf bound_ctrl:1
	s_nop 0
	v_add_f32_dpp v0, v0, v0 row_half_mirror row_mask:0xf bank_mask:0xf bound_ctrl:1
	v_add_f32_dpp v1, v1, v1 quad_perm:[2,3,0,1] row_mask:0xf bank_mask:0xf bound_ctrl:1
	s_nop 0
	v_add_f32_dpp v0, v0, v0 row_mirror row_mask:0xf bank_mask:0xf bound_ctrl:1
	v_rcp_f32_e32 v0, v0
	v_add_f32_dpp v1, v1, v1 row_half_mirror row_mask:0xf bank_mask:0xf bound_ctrl:1
	s_nop 1
	v_add_f32_dpp v1, v1, v1 row_mirror row_mask:0xf bank_mask:0xf bound_ctrl:1
	v_fmac_f32_e32 v36, v0, v1
	s_nop 0
	v_readlane_b32 s20, v36, 0
	v_readlane_b32 s23, v36, 16
	v_readlane_b32 s21, v36, 32
	v_readlane_b32 s22, v36, 48
	s_and_saveexec_b64 s[12:13], s[0:1]
	s_cbranch_execz .LBB2_8
	v_lshlrev_b64 v[0:1], 2, v[110:111]
	v_lshl_add_u64 v[2:3], s[4:5], 0, v[0:1]
	global_load_dword v4, v[2:3], off
	v_lshl_add_u64 v[2:3], s[6:7], 0, v[0:1]
	global_load_dword v5, v[2:3], off
	v_mov_b32_e32 v2, s23
	v_add_f32_e32 v2, s20, v2
	v_add_f32_e32 v2, s21, v2
	v_add_f32_e32 v2, s22, v2
	v_add_f32_e32 v6, s14, v2
	v_max_f32_e64 v7, -v6, 0
	v_mul_f32_e32 v2, 0xbfb8aa3b, v6
	v_sub_f32_e64 v8, -v6, v7
	v_exp_f32_e32 v2, v2
	v_mul_f32_e32 v3, 0xbfb8aa3b, v7
	v_mul_f32_e32 v8, 0x3fb8aa3b, v8
	v_exp_f32_e32 v3, v3
	v_exp_f32_e32 v8, v8
	v_add_f32_e32 v2, 1.0, v2
	v_rcp_f32_e32 v9, v2
	v_add_f32_e32 v2, v3, v8
	v_cmp_gt_f32_e32 vcc, s17, v2
	s_and_b64 s[20:21], vcc, exec
	s_cselect_b32 s20, 32, 0
	v_ldexp_f32 v2, v2, s20
	v_log_f32_e32 v10, v2
	v_lshl_add_u64 v[2:3], s[8:9], 0, v[0:1]
	global_store_dword v[2:3], v9, off
	v_cndmask_b32_e32 v8, 0, v118, vcc
	v_mul_f32_e32 v2, 0x3f317217, v10
	v_fma_f32 v2, v10, s18, -v2
	v_fmac_f32_e32 v2, 0x3377d1cf, v10
	v_fmac_f32_e32 v2, 0x3f317217, v10
	v_cmp_lt_f32_e64 vcc, |v10|, s19
	v_lshl_add_u64 v[0:1], s[10:11], 0, v[0:1]
	s_waitcnt vmcnt(2)
	v_fma_f32 v3, -v6, v4, v6
	v_cndmask_b32_e32 v2, v10, v2, vcc
	v_sub_f32_e32 v2, v2, v8
	v_add_f32_e32 v3, v7, v3
	v_add_f32_e32 v2, v2, v3
	s_waitcnt vmcnt(1)
	v_mul_f32_e32 v2, v5, v2
	global_store_dword v[0:1], v2, off
	s_branch .LBB2_8
